# speedup vs baseline: 1.0271x; 1.0010x over previous
.LBB2_47:
	s_mul_i32 s4, s2, 0x6000
	s_add_u32 s66, s10, s4
	s_addc_u32 s67, s11, 0
	v_cmp_gt_i32_e64 s[48:49], s3, v0
	s_and_saveexec_b64 s[4:5], s[48:49]
	s_cbranch_execz .LBB2_49
	global_load_dword v1, v8, s[66:67] nt
.LBB2_49:
	s_or_b64 exec, exec, s[4:5]
	s_min_i32 s33, s3, 0x1800
	v_or_b32_e32 v3, 0x100, v0
	v_cmp_gt_i32_e64 s[46:47], s33, v3
	v_mov_b32_e32 v38, 0
	v_mov_b32_e32 v50, 0
	s_and_saveexec_b64 s[4:5], s[46:47]
	s_cbranch_execz .LBB2_51
	global_load_dword v50, v8, s[66:67] offset:1024 nt
.LBB2_51:
	s_or_b64 exec, exec, s[4:5]
	v_or_b32_e32 v3, 0x200, v0
	v_cmp_gt_i32_e64 s[44:45], s33, v3
	s_and_saveexec_b64 s[4:5], s[44:45]
	s_cbranch_execz .LBB2_53
	global_load_dword v38, v8, s[66:67] offset:2048 nt
.LBB2_53:
	s_or_b64 exec, exec, s[4:5]
	v_or_b32_e32 v3, 0x300, v0
	v_cmp_gt_i32_e64 s[42:43], s33, v3
	v_mov_b32_e32 v37, 0
	v_mov_b32_e32 v49, 0
	s_and_saveexec_b64 s[4:5], s[42:43]
	s_cbranch_execz .LBB2_55
	global_load_dword v49, v8, s[66:67] offset:3072 nt
.LBB2_55:
	s_or_b64 exec, exec, s[4:5]
	v_or_b32_e32 v28, 0x400, v0
	v_cmp_gt_i32_e64 s[40:41], s33, v28
	s_and_saveexec_b64 s[4:5], s[40:41]
	s_cbranch_execz .LBB2_57
	v_lshlrev_b32_e32 v3, 2, v28
	global_load_dword v37, v3, s[66:67] nt
.LBB2_57:
	s_or_b64 exec, exec, s[4:5]
	v_or_b32_e32 v27, 0x500, v0
	v_cmp_gt_i32_e64 s[38:39], s33, v27
	v_mov_b32_e32 v36, 0
	v_mov_b32_e32 v48, 0
	s_and_saveexec_b64 s[4:5], s[38:39]
	s_cbranch_execz .LBB2_59
	v_lshlrev_b32_e32 v3, 2, v27
	global_load_dword v48, v3, s[66:67] nt
.LBB2_59:
	s_or_b64 exec, exec, s[4:5]
	v_or_b32_e32 v26, 0x600, v0
	v_cmp_gt_i32_e64 s[36:37], s33, v26
	s_and_saveexec_b64 s[4:5], s[36:37]
	s_cbranch_execz .LBB2_61
	v_lshlrev_b32_e32 v3, 2, v26
	global_load_dword v36, v3, s[66:67] nt
.LBB2_61:
	s_or_b64 exec, exec, s[4:5]
	v_or_b32_e32 v25, 0x700, v0
	v_cmp_gt_i32_e64 s[34:35], s33, v25
	v_mov_b32_e32 v35, 0
	v_mov_b32_e32 v47, 0
	s_and_saveexec_b64 s[4:5], s[34:35]
	s_cbranch_execz .LBB2_63
	v_lshlrev_b32_e32 v3, 2, v25
	global_load_dword v47, v3, s[66:67] nt
.LBB2_63:
	s_or_b64 exec, exec, s[4:5]
	v_or_b32_e32 v24, 0x800, v0
	v_cmp_gt_i32_e64 s[30:31], s33, v24
	s_and_saveexec_b64 s[4:5], s[30:31]
	s_cbranch_execz .LBB2_65
	v_lshlrev_b32_e32 v3, 2, v24
	global_load_dword v35, v3, s[66:67] nt
.LBB2_65:
	s_or_b64 exec, exec, s[4:5]
	v_or_b32_e32 v23, 0x900, v0
	v_cmp_gt_i32_e64 s[28:29], s33, v23
	v_mov_b32_e32 v34, 0
	v_mov_b32_e32 v46, 0
	s_and_saveexec_b64 s[4:5], s[28:29]
	s_cbranch_execz .LBB2_67
	v_lshlrev_b32_e32 v3, 2, v23
	global_load_dword v46, v3, s[66:67] nt
.LBB2_67:
	s_or_b64 exec, exec, s[4:5]
	v_or_b32_e32 v22, 0xa00, v0
	v_cmp_gt_i32_e64 s[26:27], s33, v22
	s_and_saveexec_b64 s[4:5], s[26:27]
	s_cbranch_execz .LBB2_69
	v_lshlrev_b32_e32 v3, 2, v22
	global_load_dword v34, v3, s[66:67] nt
.LBB2_69:
	s_or_b64 exec, exec, s[4:5]
	v_or_b32_e32 v21, 0xb00, v0
	v_cmp_gt_i32_e64 s[24:25], s33, v21
	v_mov_b32_e32 v33, 0
	v_mov_b32_e32 v45, 0
	s_and_saveexec_b64 s[4:5], s[24:25]
	s_cbranch_execz .LBB2_71
	v_lshlrev_b32_e32 v3, 2, v21
	global_load_dword v45, v3, s[66:67] nt
.LBB2_71:
	s_or_b64 exec, exec, s[4:5]
	v_or_b32_e32 v20, 0xc00, v0
	v_cmp_gt_i32_e64 s[22:23], s33, v20
	s_and_saveexec_b64 s[4:5], s[22:23]
	s_cbranch_execz .LBB2_73
	v_lshlrev_b32_e32 v3, 2, v20
	global_load_dword v33, v3, s[66:67] nt
.LBB2_73:
	s_or_b64 exec, exec, s[4:5]
	v_or_b32_e32 v19, 0xd00, v0
	v_cmp_gt_i32_e64 s[20:21], s33, v19
	v_mov_b32_e32 v32, 0
	v_mov_b32_e32 v44, 0
	s_and_saveexec_b64 s[4:5], s[20:21]
	s_cbranch_execz .LBB2_75
	v_lshlrev_b32_e32 v3, 2, v19
	global_load_dword v44, v3, s[66:67] nt
.LBB2_75:
	s_or_b64 exec, exec, s[4:5]
	v_or_b32_e32 v18, 0xe00, v0
	v_cmp_gt_i32_e64 s[18:19], s33, v18
	s_and_saveexec_b64 s[4:5], s[18:19]
	s_cbranch_execz .LBB2_77
	v_lshlrev_b32_e32 v3, 2, v18
	global_load_dword v32, v3, s[66:67] nt
.LBB2_77:
	s_or_b64 exec, exec, s[4:5]
	v_or_b32_e32 v17, 0xf00, v0
	v_cmp_gt_i32_e64 s[16:17], s33, v17
	v_mov_b32_e32 v31, 0
	v_mov_b32_e32 v43, 0
	s_and_saveexec_b64 s[4:5], s[16:17]
	s_cbranch_execz .LBB2_79
	v_lshlrev_b32_e32 v3, 2, v17
	global_load_dword v43, v3, s[66:67] nt
.LBB2_79:
	s_or_b64 exec, exec, s[4:5]
	v_or_b32_e32 v16, 0x1000, v0
	v_cmp_gt_i32_e64 s[14:15], s33, v16
	s_and_saveexec_b64 s[4:5], s[14:15]
	s_cbranch_execz .LBB2_81
	v_lshlrev_b32_e32 v3, 2, v16
	global_load_dword v31, v3, s[66:67] nt
.LBB2_81:
	s_or_b64 exec, exec, s[4:5]
	v_or_b32_e32 v15, 0x1100, v0
	v_cmp_gt_i32_e64 s[12:13], s33, v15
	v_mov_b32_e32 v30, 0
	v_mov_b32_e32 v42, 0
	s_and_saveexec_b64 s[4:5], s[12:13]
	s_cbranch_execz .LBB2_83
	v_lshlrev_b32_e32 v3, 2, v15
	global_load_dword v42, v3, s[66:67] nt
.LBB2_83:
	s_or_b64 exec, exec, s[4:5]
	v_or_b32_e32 v14, 0x1200, v0
	v_cmp_gt_i32_e64 s[10:11], s33, v14
	s_and_saveexec_b64 s[4:5], s[10:11]
	s_cbranch_execz .LBB2_85
	v_lshlrev_b32_e32 v3, 2, v14
	global_load_dword v30, v3, s[66:67] nt
.LBB2_85:
	s_or_b64 exec, exec, s[4:5]
	v_or_b32_e32 v13, 0x1300, v0
	v_cmp_gt_i32_e64 s[8:9], s33, v13
	v_mov_b32_e32 v29, 0
	v_mov_b32_e32 v41, 0
	s_and_saveexec_b64 s[4:5], s[8:9]
	s_cbranch_execz .LBB2_87
	v_lshlrev_b32_e32 v3, 2, v13
	global_load_dword v41, v3, s[66:67] nt
.LBB2_87:
	s_or_b64 exec, exec, s[4:5]
	v_or_b32_e32 v12, 0x1400, v0
	v_cmp_gt_i32_e64 s[6:7], s33, v12
	s_and_saveexec_b64 s[4:5], s[6:7]
	s_cbranch_execz .LBB2_89
	v_lshlrev_b32_e32 v3, 2, v12
	global_load_dword v29, v3, s[66:67] nt
.LBB2_89:
	s_or_b64 exec, exec, s[4:5]
	v_or_b32_e32 v11, 0x1500, v0
	v_cmp_gt_i32_e64 s[4:5], s33, v11
	v_mov_b32_e32 v3, 0
	v_mov_b32_e32 v40, 0
	s_and_saveexec_b64 s[50:51], s[4:5]
	s_cbranch_execz .LBB2_91
	v_lshlrev_b32_e32 v4, 2, v11
	global_load_dword v40, v4, s[66:67] nt
.LBB2_91:
	s_or_b64 exec, exec, s[50:51]
	v_or_b32_e32 v10, 0x1600, v0
	v_cmp_gt_i32_e64 s[68:69], s33, v10
	s_and_saveexec_b64 s[50:51], s[68:69]
	s_cbranch_execz .LBB2_93
	v_lshlrev_b32_e32 v3, 2, v10
	global_load_dword v3, v3, s[66:67] nt

.LBB2_172:
	v_lshlrev_b32_e32 v4, 2, v9
	global_load_dword v39, v4, s[66:67] nt
	s_or_b64 exec, exec, s[70:71]
	s_and_saveexec_b64 s[66:67], s[48:49]
	s_cbranch_execz .LBB2_95
